# DA tile loop: V-fragment LDS reads hoisted ahead of the PV bursts (deferred half: before the step barrier; immediate half: at the head of the exp block, PV leads with the resident k-step); m1
# speedup vs baseline: 1.0139x; 1.0139x over previous
; #define SBAR() __builtin_amdgcn_sched_barrier(0)
; #define ATT_RDK(X, KS) do { X##0 = tr_read<v_rd_off(0, KS, 0)>(vb); X##1 = tr_read<v_rd_off(0, KS, 1)>(vb); X##2 = tr_read<v_rd_off(1, KS, 0)>(vb); X##3 = tr_read<v_rd_off(1, KS, 1)>(vb); \
;     X##4 = tr_read<v_rd_off(2, KS, 0)>(vb); X##5 = tr_read<v_rd_off(2, KS, 1)>(vb); X##6 = tr_read<v_rd_off(3, KS, 0)>(vb); X##7 = tr_read<v_rd_off(3, KS, 1)>(vb); } while (0)
; #define ATT_MMAK(PA, X) do { o[0] = __builtin_amdgcn_mfma_f32_32x32x16_bf16(PA, ATT_PKV(X##0, X##1), o[0], 0, 0, 0); o[1] = __builtin_amdgcn_mfma_f32_32x32x16_bf16(PA, ATT_PKV(X##2, X##3), o[1], 0, 0, 0); \
;     o[2] = __builtin_amdgcn_mfma_f32_32x32x16_bf16(PA, ATT_PKV(X##4, X##5), o[2], 0, 0, 0); o[3] = __builtin_amdgcn_mfma_f32_32x32x16_bf16(PA, ATT_PKV(X##6, X##7), o[3], 0, 0, 0); } while (0)
; __device__ __forceinline__ void pv_pipe(f32x16* o, int vb, bf16x8 pa0, bf16x8 pa1, bf16x8 pa2, bf16x8 pa3) {
;     s16x4 a0, a1, a2, a3, a4, a5, a6, a7, b0, b1, b2, b3, b4, b5, b6, b7;
;     SBAR(); ATT_RDK(a, 0); ATT_RDK(b, 1);
;     asm volatile("s_waitcnt lgkmcnt(8)" ::: "memory"); SBAR(); ATT_MMAK(pa0, a);
;     SBAR(); ATT_RDK(a, 2);
;     asm volatile("s_waitcnt lgkmcnt(8)" ::: "memory"); SBAR(); ATT_MMAK(pa1, b);
;     SBAR(); ATT_RDK(b, 3);
;     asm volatile("s_waitcnt lgkmcnt(8)" ::: "memory"); SBAR(); ATT_MMAK(pa2, a);
;     asm volatile("s_waitcnt lgkmcnt(0)" ::: "memory"); SBAR(); ATT_MMAK(pa3, b);
; }
; __device__ __forceinline__ void da_unit(LAS unsigned char* lds, const bf16* __restrict__ Q, const bf16* __restrict__ Kp, const bf16* __restrict__ Vp, const float* __restrict__ gda, float lam, ...
;     ...
;             if (comp == 0) pv_pipe(o, vb0 + vbuf * SHM_T, pa0, pa1, pa2, pa3); else { pend = true; pbuf = vbuf; }
.LBB0_572:
	ds_read_b64_tr_b16 v[100:101], v250 offset:0
	ds_read_b64_tr_b16 v[102:103], v250 offset:0x800
	ds_read_b64_tr_b16 v[104:105], v250 offset:0x200
	ds_read_b64_tr_b16 v[106:107], v250 offset:0xa00
	ds_read_b64_tr_b16 v[108:109], v250 offset:0x400
	ds_read_b64_tr_b16 v[110:111], v250 offset:0xc00
	ds_read_b64_tr_b16 v[184:185], v250 offset:0x600
	ds_read_b64_tr_b16 v[186:187], v250 offset:0xe00
	s_waitcnt lgkmcnt(8)
	s_nop 0
	s_setprio 1
	v_mfma_f32_32x32x16_bf16 v[2:17], v[94:97], v[188:191], v[2:17]
	v_mfma_f32_32x32x16_bf16 v[18:33], v[94:97], v[196:199], v[18:33]
	v_mfma_f32_32x32x16_bf16 v[34:49], v[94:97], v[200:203], v[34:49]
	v_mfma_f32_32x32x16_bf16 v[50:65], v[94:97], v[204:207], v[50:65]
	ds_read_b64_tr_b16 v[188:189], v250 offset:0x3000
	ds_read_b64_tr_b16 v[190:191], v250 offset:0x3800
	ds_read_b64_tr_b16 v[196:197], v250 offset:0x3200
	ds_read_b64_tr_b16 v[198:199], v250 offset:0x3a00
	ds_read_b64_tr_b16 v[200:201], v250 offset:0x3400
	ds_read_b64_tr_b16 v[202:203], v250 offset:0x3c00
	ds_read_b64_tr_b16 v[204:205], v250 offset:0x3600
	ds_read_b64_tr_b16 v[206:207], v250 offset:0x3e00
	s_waitcnt lgkmcnt(8)
	v_mfma_f32_32x32x16_bf16 v[2:17], v[86:89], v[100:103], v[2:17]
	v_mfma_f32_32x32x16_bf16 v[18:33], v[86:89], v[104:107], v[18:33]
	v_mfma_f32_32x32x16_bf16 v[34:49], v[86:89], v[108:111], v[34:49]
	v_mfma_f32_32x32x16_bf16 v[50:65], v[86:89], v[184:187], v[50:65]
	ds_read_b64_tr_b16 v[100:101], v250 offset:0x2000
	ds_read_b64_tr_b16 v[102:103], v250 offset:0x2800
	ds_read_b64_tr_b16 v[104:105], v250 offset:0x2200
	ds_read_b64_tr_b16 v[106:107], v250 offset:0x2a00
	ds_read_b64_tr_b16 v[108:109], v250 offset:0x2400
	ds_read_b64_tr_b16 v[110:111], v250 offset:0x2c00
	ds_read_b64_tr_b16 v[184:185], v250 offset:0x2600
	ds_read_b64_tr_b16 v[186:187], v250 offset:0x2e00
	s_waitcnt lgkmcnt(8)
	v_mfma_f32_32x32x16_bf16 v[2:17], v[82:85], v[188:191], v[2:17]
	s_waitcnt lgkmcnt(0)
	v_mfma_f32_32x32x16_bf16 v[18:33], v[82:85], v[196:199], v[18:33]
	v_mfma_f32_32x32x16_bf16 v[34:49], v[82:85], v[200:203], v[34:49]
	v_mfma_f32_32x32x16_bf16 v[50:65], v[82:85], v[204:207], v[50:65]
	v_mfma_f32_32x32x16_bf16 v[2:17], v[90:93], v[100:103], v[2:17]
	v_mfma_f32_32x32x16_bf16 v[18:33], v[90:93], v[104:107], v[18:33]
	v_mfma_f32_32x32x16_bf16 v[34:49], v[90:93], v[108:111], v[34:49]
	v_mfma_f32_32x32x16_bf16 v[50:65], v[90:93], v[184:187], v[50:65]
	s_setprio 0

; #define SBAR() __builtin_amdgcn_sched_barrier(0)
; #define ATT_RDK(X, KS) do { X##0 = tr_read<v_rd_off(0, KS, 0)>(vb); X##1 = tr_read<v_rd_off(0, KS, 1)>(vb); X##2 = tr_read<v_rd_off(1, KS, 0)>(vb); X##3 = tr_read<v_rd_off(1, KS, 1)>(vb); \
;     X##4 = tr_read<v_rd_off(2, KS, 0)>(vb); X##5 = tr_read<v_rd_off(2, KS, 1)>(vb); X##6 = tr_read<v_rd_off(3, KS, 0)>(vb); X##7 = tr_read<v_rd_off(3, KS, 1)>(vb); } while (0)
; __device__ __forceinline__ void pv_pipe(f32x16* o, int vb, bf16x8 pa0, bf16x8 pa1, bf16x8 pa2, bf16x8 pa3) {
;     s16x4 a0, a1, a2, a3, a4, a5, a6, a7, b0, b1, b2, b3, b4, b5, b6, b7;
;     SBAR(); ATT_RDK(a, 0); ATT_RDK(b, 1);
; __device__ __forceinline__ void da_unit(LAS unsigned char* lds, const bf16* __restrict__ Q, const bf16* __restrict__ Kp, const bf16* __restrict__ Vp, const float* __restrict__ gda, float lam, ...
;     ...
;         if (comp == 1 && pend) { pv_pipe(o, vb0 + pbuf * SHM_T, pa0, pa1, pa2, pa3); pend = false; }
.LBB0_579:
	s_and_b64 s[8:9], s[12:13], s[18:19]
	s_cbranch_scc0 .Lda_nopre
	v_lshl_add_u32 v195, s25, 14, v169
	ds_read_b64_tr_b16 v[98:99], v195 offset:0
	ds_read_b64_tr_b16 v[100:101], v195 offset:0x800
	ds_read_b64_tr_b16 v[102:103], v195 offset:0x200
	ds_read_b64_tr_b16 v[104:105], v195 offset:0xa00
	ds_read_b64_tr_b16 v[106:107], v195 offset:0x400
	ds_read_b64_tr_b16 v[108:109], v195 offset:0xc00
	ds_read_b64_tr_b16 v[110:111], v195 offset:0x600
	ds_read_b64_tr_b16 v[112:113], v195 offset:0xe00
	ds_read_b64_tr_b16 v[182:183], v195 offset:0x1000
	ds_read_b64_tr_b16 v[184:185], v195 offset:0x1800
	ds_read_b64_tr_b16 v[186:187], v195 offset:0x1200
	ds_read_b64_tr_b16 v[188:189], v195 offset:0x1a00
	ds_read_b64_tr_b16 v[190:191], v195 offset:0x1400
	ds_read_b64_tr_b16 v[192:193], v195 offset:0x1c00
	ds_read_b64_tr_b16 v[196:197], v195 offset:0x1600
	ds_read_b64_tr_b16 v[198:199], v195 offset:0x1e00

; #define SBAR() __builtin_amdgcn_sched_barrier(0)
; #define ATT_RDK(X, KS) do { X##0 = tr_read<v_rd_off(0, KS, 0)>(vb); X##1 = tr_read<v_rd_off(0, KS, 1)>(vb); X##2 = tr_read<v_rd_off(1, KS, 0)>(vb); X##3 = tr_read<v_rd_off(1, KS, 1)>(vb); \
;     X##4 = tr_read<v_rd_off(2, KS, 0)>(vb); X##5 = tr_read<v_rd_off(2, KS, 1)>(vb); X##6 = tr_read<v_rd_off(3, KS, 0)>(vb); X##7 = tr_read<v_rd_off(3, KS, 1)>(vb); } while (0)
; #define ATT_MMAK(PA, X) do { o[0] = __builtin_amdgcn_mfma_f32_32x32x16_bf16(PA, ATT_PKV(X##0, X##1), o[0], 0, 0, 0); o[1] = __builtin_amdgcn_mfma_f32_32x32x16_bf16(PA, ATT_PKV(X##2, X##3), o[1], 0, 0, 0); \
;     o[2] = __builtin_amdgcn_mfma_f32_32x32x16_bf16(PA, ATT_PKV(X##4, X##5), o[2], 0, 0, 0); o[3] = __builtin_amdgcn_mfma_f32_32x32x16_bf16(PA, ATT_PKV(X##6, X##7), o[3], 0, 0, 0); } while (0)
; __device__ __forceinline__ void pv_pipe(f32x16* o, int vb, bf16x8 pa0, bf16x8 pa1, bf16x8 pa2, bf16x8 pa3) {
;     s16x4 a0, a1, a2, a3, a4, a5, a6, a7, b0, b1, b2, b3, b4, b5, b6, b7;
;     SBAR(); ATT_RDK(a, 0); ATT_RDK(b, 1);
;     asm volatile("s_waitcnt lgkmcnt(8)" ::: "memory"); SBAR(); ATT_MMAK(pa0, a);
;     SBAR(); ATT_RDK(a, 2);
;     asm volatile("s_waitcnt lgkmcnt(8)" ::: "memory"); SBAR(); ATT_MMAK(pa1, b);
;     SBAR(); ATT_RDK(b, 3);
;     asm volatile("s_waitcnt lgkmcnt(8)" ::: "memory"); SBAR(); ATT_MMAK(pa2, a);
;     asm volatile("s_waitcnt lgkmcnt(0)" ::: "memory"); SBAR(); ATT_MMAK(pa3, b);
; }
; __device__ __forceinline__ void da_unit(LAS unsigned char* lds, const bf16* __restrict__ Q, const bf16* __restrict__ Kp, const bf16* __restrict__ Vp, const float* __restrict__ gda, float lam, ...
;     ...
;         if (comp == 1 && pend) { pv_pipe(o, vb0 + pbuf * SHM_T, pa0, pa1, pa2, pa3); pend = false; }
.LBB0_583:
	s_waitcnt lgkmcnt(8)
	s_nop 0
	s_setprio 1
	v_mfma_f32_32x32x16_bf16 v[2:17], v[86:89], v[98:101], v[2:17]
	v_mfma_f32_32x32x16_bf16 v[18:33], v[86:89], v[102:105], v[18:33]
	v_mfma_f32_32x32x16_bf16 v[34:49], v[86:89], v[106:109], v[34:49]
	v_mfma_f32_32x32x16_bf16 v[50:65], v[86:89], v[110:113], v[50:65]
	ds_read_b64_tr_b16 v[98:99], v195 offset:0x2000
	ds_read_b64_tr_b16 v[100:101], v195 offset:0x2800
	ds_read_b64_tr_b16 v[102:103], v195 offset:0x2200
	ds_read_b64_tr_b16 v[104:105], v195 offset:0x2a00
	ds_read_b64_tr_b16 v[106:107], v195 offset:0x2400
	ds_read_b64_tr_b16 v[108:109], v195 offset:0x2c00
	ds_read_b64_tr_b16 v[110:111], v195 offset:0x2600
	ds_read_b64_tr_b16 v[112:113], v195 offset:0x2e00
	s_waitcnt lgkmcnt(8)
	v_mfma_f32_32x32x16_bf16 v[2:17], v[94:97], v[182:185], v[2:17]
	v_mfma_f32_32x32x16_bf16 v[18:33], v[94:97], v[186:189], v[18:33]
	v_mfma_f32_32x32x16_bf16 v[34:49], v[94:97], v[190:193], v[34:49]
	v_mfma_f32_32x32x16_bf16 v[50:65], v[94:97], v[196:199], v[50:65]
	ds_read_b64_tr_b16 v[182:183], v195 offset:0x3000
	ds_read_b64_tr_b16 v[184:185], v195 offset:0x3800
	ds_read_b64_tr_b16 v[186:187], v195 offset:0x3200
	ds_read_b64_tr_b16 v[188:189], v195 offset:0x3a00
	ds_read_b64_tr_b16 v[190:191], v195 offset:0x3400
	ds_read_b64_tr_b16 v[192:193], v195 offset:0x3c00
	ds_read_b64_tr_b16 v[196:197], v195 offset:0x3600
	ds_read_b64_tr_b16 v[198:199], v195 offset:0x3e00
	s_waitcnt lgkmcnt(8)
	v_mfma_f32_32x32x16_bf16 v[2:17], v[90:93], v[98:101], v[2:17]
	s_waitcnt lgkmcnt(0)
	v_mfma_f32_32x32x16_bf16 v[18:33], v[90:93], v[102:105], v[18:33]
	v_mfma_f32_32x32x16_bf16 v[34:49], v[90:93], v[106:109], v[34:49]
	v_mfma_f32_32x32x16_bf16 v[50:65], v[90:93], v[110:113], v[50:65]
	v_mfma_f32_32x32x16_bf16 v[2:17], v[82:85], v[182:185], v[2:17]
	s_mov_b64 s[18:19], 0
	v_mfma_f32_32x32x16_bf16 v[18:33], v[82:85], v[186:189], v[18:33]
	v_mfma_f32_32x32x16_bf16 v[34:49], v[82:85], v[190:193], v[34:49]
	v_mfma_f32_32x32x16_bf16 v[50:65], v[82:85], v[196:199], v[50:65]
	s_setprio 0
	s_add_i32 s8, s27, 3
	s_cmp_ge_u32 s8, s26
	s_cbranch_scc1 .LBB0_574

; __device__ __forceinline__ int crow(int r, int hi) { return (r & 3) + 8 * (r >> 2) + 4 * hi; }
; __device__ __forceinline__ void da_unit(LAS unsigned char* lds, const bf16* __restrict__ Q, const bf16* __restrict__ Kp, const bf16* __restrict__ Vp, const float* __restrict__ gda, float lam, ...
;     ...
;             for (int r = 0; r < 16; ++r) { p0[r] = __builtin_amdgcn_exp2f(p0[r]); p1[r] = __builtin_amdgcn_exp2f(p1[r]); }
;             if (__any(alpha < 1.f)) { if (hi == 0) al_l[r32] = alpha; asm volatile("s_waitcnt lgkmcnt(0)" ::: "memory");
; #pragma unroll
;                 for (int r = 0; r < 16; ++r) { const float al = al_l[crow(r, hi)];
; #pragma unroll
;                     for (int d = 0; d < 4; ++d) o[d][r] *= al; } }
;             float ps = 0.f;
; #pragma unroll
;             for (int r = 0; r < 16; ++r) ps += p0[r];
; #pragma unroll
;             for (int r = 0; r < 16; ++r) ps += p1[r];
;             { auto rr = __builtin_amdgcn_permlane32_swap(__builtin_bit_cast(unsigned, ps), __builtin_bit_cast(unsigned, ps), false, false);
;               ps = __builtin_bit_cast(float, rr[0]) + __builtin_bit_cast(float, rr[1]); }
;             l_reg = l_reg * alpha + ps;
;             ATT_PK4(p0, 0, pa0); ATT_PK4(p0, 8, pa1); ATT_PK4(p1, 0, pa2); ATT_PK4(p1, 8, pa3);
;             if (comp == 0) pv_pipe(o, vb0 + vbuf * SHM_T, pa0, pa1, pa2, pa3); else { pend = true; pbuf = vbuf; }
.LBB0_590:
	s_and_b64 vcc, exec, s[44:45]
	s_cbranch_vccz .Lda_nog2
	v_lshl_add_u32 v250, s29, 14, v169
	ds_read_b64_tr_b16 v[188:189], v250 offset:0x1000
	ds_read_b64_tr_b16 v[190:191], v250 offset:0x1800
	ds_read_b64_tr_b16 v[196:197], v250 offset:0x1200
	ds_read_b64_tr_b16 v[198:199], v250 offset:0x1a00
	ds_read_b64_tr_b16 v[200:201], v250 offset:0x1400
	ds_read_b64_tr_b16 v[202:203], v250 offset:0x1c00
	ds_read_b64_tr_b16 v[204:205], v250 offset:0x1600
	ds_read_b64_tr_b16 v[206:207], v250 offset:0x1e00
.Lda_nog2:
	v_exp_f32_e32 v82, v82
	v_exp_f32_e32 v83, v83
	v_exp_f32_e32 v84, v84
	v_exp_f32_e32 v85, v85
	v_exp_f32_e32 v184, v86
	v_add_f32_e32 v86, 0, v82
	v_exp_f32_e32 v185, v87
	v_add_f32_e32 v86, v83, v86
	v_exp_f32_e32 v186, v88
	v_add_f32_e32 v86, v84, v86
	v_exp_f32_e32 v89, v89
	v_add_f32_e32 v86, v85, v86
	v_exp_f32_e32 v90, v90
	v_add_f32_e32 v86, v184, v86
	v_exp_f32_e32 v91, v91
	v_add_f32_e32 v86, v185, v86
	v_exp_f32_e32 v92, v92
	v_add_f32_e32 v86, v186, v86
	v_exp_f32_e32 v93, v93
	v_add_f32_e32 v86, v89, v86
	v_exp_f32_e32 v187, v94
	v_add_f32_e32 v86, v90, v86
	v_exp_f32_e32 v208, v95
	v_add_f32_e32 v86, v91, v86
	v_exp_f32_e32 v209, v96
	v_add_f32_e32 v86, v92, v86
	v_exp_f32_e32 v97, v97
	v_add_f32_e32 v86, v93, v86
	v_exp_f32_e32 v183, v98
	v_add_f32_e32 v86, v187, v86
	v_exp_f32_e32 v99, v99
	v_add_f32_e32 v86, v208, v86
	v_exp_f32_e32 v100, v100
	v_add_f32_e32 v86, v209, v86
	v_exp_f32_e32 v101, v101
	v_add_f32_e32 v86, v97, v86
	v_exp_f32_e32 v102, v102
	v_add_f32_e32 v86, v183, v86
	v_exp_f32_e32 v103, v103
	v_add_f32_e32 v86, v99, v86
	v_exp_f32_e32 v104, v104
	v_add_f32_e32 v86, v100, v86
	v_exp_f32_e32 v105, v105
	v_add_f32_e32 v86, v101, v86
	v_exp_f32_e32 v106, v106
	v_add_f32_e32 v86, v102, v86
	v_exp_f32_e32 v107, v107
	v_add_f32_e32 v86, v103, v86
	v_exp_f32_e32 v108, v108
	v_add_f32_e32 v86, v104, v86
	v_exp_f32_e32 v109, v109
	v_add_f32_e32 v86, v105, v86
	v_exp_f32_e32 v110, v110
	v_add_f32_e32 v86, v106, v86
	v_exp_f32_e32 v111, v111
	v_add_f32_e32 v86, v107, v86
	v_exp_f32_e32 v112, v112
	v_add_f32_e32 v86, v108, v86
	v_exp_f32_e32 v113, v113
	v_add_f32_e32 v86, v109, v86
	v_add_f32_e32 v86, v110, v86
	v_add_f32_e32 v86, v111, v86
	v_add_f32_e32 v86, v112, v86
	v_add_f32_e32 v98, v113, v86
	v_mov_b32_e32 v86, v98
	s_nop 1
	v_permlane32_swap_b32_e32 v98, v86
	v_cvt_pk_bf16_f32 v86, v82, v83
	v_cvt_pk_bf16_f32 v87, v84, v85
	v_cvt_pk_bf16_f32 v88, v184, v185
	v_cvt_pk_bf16_f32 v89, v186, v89
	v_cvt_pk_bf16_f32 v94, v90, v91
	v_cvt_pk_bf16_f32 v95, v92, v93
	v_cvt_pk_bf16_f32 v96, v187, v208
	v_cvt_pk_bf16_f32 v97, v209, v97
	v_cvt_pk_bf16_f32 v90, v183, v99
	v_cvt_pk_bf16_f32 v91, v100, v101
	v_cvt_pk_bf16_f32 v92, v102, v103
	v_cvt_pk_bf16_f32 v93, v104, v105
	v_cvt_pk_bf16_f32 v82, v106, v107
	v_cvt_pk_bf16_f32 v83, v108, v109
	v_cvt_pk_bf16_f32 v84, v110, v111
	v_cvt_pk_bf16_f32 v85, v112, v113
	v_permlane32_swap_b32_e32 v86, v88
	v_permlane32_swap_b32_e32 v87, v89
	v_permlane32_swap_b32_e32 v94, v96
	v_permlane32_swap_b32_e32 v95, v97
	v_permlane32_swap_b32_e32 v90, v92
	v_permlane32_swap_b32_e32 v91, v93
	v_permlane32_swap_b32_e32 v82, v84
	s_andn2_b64 vcc, exec, s[44:45]
	v_permlane32_swap_b32_e32 v83, v85
	s_cbranch_vccz .LBB0_572
	s_mov_b64 s[18:19], -1
	s_mov_b32 s25, s29
	s_branch .LBB0_573
